# C2/C3 unit loops: first two sub-phases after an epilogue peeled with vmcnt(8+S) so the epilogue stores need not retire before the next unit's first MFMAs
# baseline (speedup 1.0000x reference)
; #define PG8_STAGE_B(bufoff, gbase) do { _Pragma("unroll") for (int _i = 0; _i < 2; ++_i) { unsigned _o = voffB[_i]; asm volatile("" : "+v"(_o)); \
;         __builtin_amdgcn_global_load_lds((const unsigned*)((const char*)(gbase) + _o), (LAS unsigned*)(lds + (bufoff) + ldsw + _i * 8192), 16, 0, 0); } } while (0)
; #define PG8_STAGE_A(bufoff, gbase, h) do { _Pragma("unroll") for (int _i = 0; _i < 2; ++_i) { unsigned _o = (GATHER ? aoffs[h][_i] : voffA[_i]); asm volatile("" : "+v"(_o)); \
;         __builtin_amdgcn_global_load_lds((const unsigned*)((const char*)(gbase) + _o), (LAS unsigned*)(lds + (bufoff) + ldsw + _i * 8192), 16, 0, 0); } } while (0)
; #define PG8_GOFFS(u) do { if constexpr (GATHER) { _Pragma("unroll") for (int _i = 0; _i < 2; ++_i) { int _R, _C; stage_rc(tid * 16 + _i * 8192, _R, _C); \
;         aoffs[0][_i] = (unsigned)gtab[(u) * 256 + _R] * (unsigned)(K * ES) + (unsigned)(_C * 2); aoffs[1][_i] = (unsigned)gtab[(u) * 256 + 128 + _R] * (unsigned)(K * ES) + (unsigned)(_C * 2); } } } while (0)
; #define PG8_BAR __builtin_amdgcn_s_barrier()
; template <int K, bool PERM, bool GATHER, int MODE  , class Sched, class Epi>
; __device__ __forceinline__ void gemm_phase(LAS unsigned char* lds, const Sched& S, const Epi& E, const LAS int* gtab, int wv) {
;     ...
;         const bool has_next = S.next(ui + 1, nxt);
;         const char* nA = has_next ? nxt.A : cA; const char* nB = has_next ? nxt.B : cB;
; #pragma clang loop unroll(disable)
;         for (int t = 0; t < nt; t += 2) {
;             const bool last = (t == nt - 2);
;             const char* a1 = cA + (size_t)(t + 1) * kstep;
;             const char* a2 = last ? nA : cA + (size_t)(t + 2) * kstep;
;             const char* b2 = last ? nB : cB + (size_t)(t + 2) * kstep;
;             const char* a3 = a2 + kstep; const char* b3 = b2 + kstep;
;             PG8_LDB(B0, 0, 0); PG8_LDB(B1, 0, 1); PG8_SCHED; PG8_LDA(At, 0, 0); PG8_STAGE_A(PG8_SA(1, 1), a1 + hstep, 1);
;             PG8_WAIT_V(8); PG8_WAIT_L(0); PG8_BAR; PG8_MMA(0, 0, At, B0); PG8_MMA(0, 1, At, B1); PG8_BAR; PG8_SCHED;
;             if (last && has_next) PG8_GOFFS(ui + 1);
;             PG8_LDA(At, 0, 1); PG8_STAGE_B(PG8_SB(0, 0), b2); PG8_STAGE_B(PG8_SB(0, 1), b2 + BH); PG8_STAGE_A(PG8_SA(0, 0), a2, 0);
;             PG8_WAIT_V(8); PG8_WAIT_L(0); PG8_BAR; PG8_MMA(1, 0, At, B0); PG8_MMA(1, 1, At, B1); PG8_BAR; PG8_SCHED;
.LBB0_744:
	s_xor_b64 s[14:15], s[16:17], -1
	s_add_u32 s85, s18, 0x100
	s_addc_u32 s86, s19, 0
	s_and_b64 s[22:23], s[16:17], exec
	s_cselect_b32 s87, s1, s1
	s_cselect_b32 s88, s0, s0
	s_cselect_b32 s89, s13, s19
	s_cselect_b32 s90, s12, s18
	s_lshl_b32 s18, s79, 10
	s_add_i32 s18, s18, 0
	s_add_i32 s22, s18, 0x20000
	s_cmp_gt_i32 s28, -1
	s_cselect_b64 s[18:19], -1, 0
	v_lshl_add_u32 v171, v155, 2, s22
	v_lshl_add_u32 v172, v158, 2, s22
	s_lshl_b64 s[22:23], s[28:29], 2
	s_add_u32 s22, s69, s22
	s_addc_u32 s23, s72, s23
	s_mov_b32 s91, -2
	s_cmp_gt_i32 s28, -1
	s_cbranch_scc0 .LBB0_747
	v_add_u32_e32 v0, v166, v165
	ds_read_b128 v[12:15], v166
	ds_read_b64 v[16:17], v0 offset:1024
	ds_read_b128 v[18:21], v166 offset:2048
	ds_read_b64 v[22:23], v0 offset:3072
	ds_read_b128 v[0:3], v167
	v_add_u32_e32 v10, v167, v165
	ds_read_b64 v[4:5], v10 offset:1024
	ds_read_b128 v[6:9], v167 offset:2048
	ds_read_b64 v[10:11], v10 offset:3072
	s_cmpk_eq_i32 s20, 0x300
	s_cselect_b64 s[26:27], -1, 0
	s_add_u32 s24, s0, s20
	v_add_u32_e32 v173, v168, v165
	s_addc_u32 s25, s1, s21
	ds_read_b128 v[192:195], v168
	ds_read_b64 v[196:197], v173 offset:1024
	ds_read_b128 v[198:201], v168 offset:2048
	ds_read_b64 v[202:203], v173 offset:3072
	ds_read_b128 v[204:207], v168 offset:4096
	ds_read_b64 v[208:209], v173 offset:5120
	ds_read_b128 v[210:213], v168 offset:6144
	ds_read_b64 v[214:215], v173 offset:7168
	s_add_u32 s30, s24, 0x80
	s_addc_u32 s31, s25, 0
	s_add_i32 m0, s3, 0xc000
	s_nop 0
	global_load_lds_dwordx4 v162, s[30:31]
	s_add_i32 m0, s3, 0xe000
	s_nop 0
	global_load_lds_dwordx4 v164, s[30:31]
	s_waitcnt vmcnt(12)
	s_waitcnt lgkmcnt(0)
	s_barrier
	s_setprio 1
	s_waitcnt lgkmcnt(0)
	v_mfma_f32_16x16x128_f8f6f4 v[148:151], v[12:17], v[192:197], v[148:151] cbsz:2 blgp:2
	v_mfma_f32_16x16x128_f8f6f4 v[144:147], v[18:23], v[192:197], v[144:147] cbsz:2 blgp:2
	v_mfma_f32_16x16x128_f8f6f4 v[140:143], v[12:17], v[198:203], v[140:143] cbsz:2 blgp:2
	v_mfma_f32_16x16x128_f8f6f4 v[136:139], v[18:23], v[198:203], v[136:139] cbsz:2 blgp:2
	v_mfma_f32_16x16x128_f8f6f4 v[132:135], v[12:17], v[204:209], v[132:135] cbsz:2 blgp:2
	v_mfma_f32_16x16x128_f8f6f4 v[128:131], v[18:23], v[204:209], v[128:131] cbsz:2 blgp:2
	v_mfma_f32_16x16x128_f8f6f4 v[124:127], v[12:17], v[210:215], v[124:127] cbsz:2 blgp:2
	v_mfma_f32_16x16x128_f8f6f4 v[120:123], v[18:23], v[210:215], v[120:123] cbsz:2 blgp:2
	s_setprio 0
	s_setprio 1
	v_mfma_f32_16x16x128_f8f6f4 v[116:119], v[0:5], v[192:197], v[116:119] cbsz:2 blgp:2
	v_mfma_f32_16x16x128_f8f6f4 v[112:115], v[6:11], v[192:197], v[112:115] cbsz:2 blgp:2
	v_mfma_f32_16x16x128_f8f6f4 v[108:111], v[0:5], v[198:203], v[108:111] cbsz:2 blgp:2
	v_mfma_f32_16x16x128_f8f6f4 v[104:107], v[6:11], v[198:203], v[104:107] cbsz:2 blgp:2
	v_mfma_f32_16x16x128_f8f6f4 v[100:103], v[0:5], v[204:209], v[100:103] cbsz:2 blgp:2
	v_mfma_f32_16x16x128_f8f6f4 v[96:99], v[6:11], v[204:209], v[96:99] cbsz:2 blgp:2
	v_mfma_f32_16x16x128_f8f6f4 v[92:95], v[0:5], v[210:215], v[92:95] cbsz:2 blgp:2
	v_mfma_f32_16x16x128_f8f6f4 v[88:91], v[6:11], v[210:215], v[88:91] cbsz:2 blgp:2
	s_setprio 0
	s_barrier
	s_and_b64 s[24:25], s[16:17], s[26:27]
	s_andn2_b64 vcc, exec, s[24:25]
	s_cbranch_vccnz .Lc2p_sp2
	ds_read2st64_b32 v[162:163], v171 offset1:2
	ds_read2st64_b32 v[174:175], v172 offset1:2
	s_waitcnt lgkmcnt(0)
	v_lshl_add_u32 v161, v162, 10, v156
	v_lshl_add_u32 v162, v163, 10, v156
	v_lshl_add_u32 v163, v174, 10, v159
	v_lshl_add_u32 v164, v175, 10, v159
.Lc2p_sp2:
	s_add_u32 s24, s0, s20
	s_addc_u32 s25, s1, s21
	s_add_u32 s30, s24, 0x100
	s_addc_u32 s31, s25, 0
	s_and_b64 s[24:25], s[26:27], exec
	s_cselect_b32 s25, s87, s31
	s_cselect_b32 s24, s88, s30
	s_add_u32 s30, s85, s20
	s_addc_u32 s31, s86, s21
	s_and_b64 s[26:27], s[26:27], exec
	s_mov_b32 m0, s58
	s_cselect_b32 s27, s89, s31
	s_cselect_b32 s26, s90, s30
	ds_read_b128 v[192:195], v168 offset:16384
	ds_read_b64 v[196:197], v173 offset:17408
	ds_read_b128 v[198:201], v168 offset:18432
	ds_read_b64 v[202:203], v173 offset:19456
	ds_read_b128 v[204:207], v168 offset:20480
	ds_read_b64 v[208:209], v173 offset:21504
	ds_read_b128 v[210:213], v168 offset:22528
	ds_read_b64 v[214:215], v173 offset:23552
	s_add_u32 s30, s26, 0x100000
	global_load_lds_dwordx4 v157, s[26:27]
	s_mov_b32 m0, s59
	s_addc_u32 s31, s27, 0
	global_load_lds_dwordx4 v160, s[26:27]
	s_mov_b32 m0, s64
	s_nop 0
	global_load_lds_dwordx4 v157, s[30:31]
	s_mov_b32 m0, s65
	s_nop 0
	global_load_lds_dwordx4 v160, s[30:31]
	s_mov_b32 m0, s3
	s_nop 0
	global_load_lds_dwordx4 v161, s[24:25]
	s_mov_b32 m0, s66
	s_nop 0
	global_load_lds_dwordx4 v163, s[24:25]
	s_waitcnt vmcnt(12)
	s_waitcnt lgkmcnt(0)
	s_barrier
	s_setprio 1
	s_waitcnt lgkmcnt(0)
	v_mfma_f32_16x16x128_f8f6f4 v[84:87], v[12:17], v[192:197], v[84:87] cbsz:2 blgp:2
	v_mfma_f32_16x16x128_f8f6f4 v[80:83], v[18:23], v[192:197], v[80:83] cbsz:2 blgp:2
	v_mfma_f32_16x16x128_f8f6f4 v[76:79], v[12:17], v[198:203], v[76:79] cbsz:2 blgp:2
	v_mfma_f32_16x16x128_f8f6f4 v[72:75], v[18:23], v[198:203], v[72:75] cbsz:2 blgp:2
	v_mfma_f32_16x16x128_f8f6f4 v[68:71], v[12:17], v[204:209], v[68:71] cbsz:2 blgp:2
	v_mfma_f32_16x16x128_f8f6f4 v[64:67], v[18:23], v[204:209], v[64:67] cbsz:2 blgp:2
	v_mfma_f32_16x16x128_f8f6f4 v[60:63], v[12:17], v[210:215], v[60:63] cbsz:2 blgp:2
	v_mfma_f32_16x16x128_f8f6f4 v[56:59], v[18:23], v[210:215], v[56:59] cbsz:2 blgp:2
	s_setprio 0
	s_setprio 1
	v_mfma_f32_16x16x128_f8f6f4 v[52:55], v[0:5], v[192:197], v[52:55] cbsz:2 blgp:2
	v_mfma_f32_16x16x128_f8f6f4 v[48:51], v[6:11], v[192:197], v[48:51] cbsz:2 blgp:2
	v_mfma_f32_16x16x128_f8f6f4 v[44:47], v[0:5], v[198:203], v[44:47] cbsz:2 blgp:2
	v_mfma_f32_16x16x128_f8f6f4 v[40:43], v[6:11], v[198:203], v[40:43] cbsz:2 blgp:2
	v_mfma_f32_16x16x128_f8f6f4 v[36:39], v[0:5], v[204:209], v[36:39] cbsz:2 blgp:2
	v_mfma_f32_16x16x128_f8f6f4 v[32:35], v[6:11], v[204:209], v[32:35] cbsz:2 blgp:2
	v_mfma_f32_16x16x128_f8f6f4 v[28:31], v[0:5], v[210:215], v[28:31] cbsz:2 blgp:2
	v_mfma_f32_16x16x128_f8f6f4 v[24:27], v[6:11], v[210:215], v[24:27] cbsz:2 blgp:2
	s_setprio 0
	s_barrier
	s_branch .Lc2_mid

; #define PG8_STAGE_A(bufoff, gbase, h) do { _Pragma("unroll") for (int _i = 0; _i < 2; ++_i) { unsigned _o = (GATHER ? aoffs[h][_i] : voffA[_i]); asm volatile("" : "+v"(_o)); \
;         __builtin_amdgcn_global_load_lds((const unsigned*)((const char*)(gbase) + _o), (LAS unsigned*)(lds + (bufoff) + ldsw + _i * 8192), 16, 0, 0); } } while (0)
; #define PG8_WAIT_V(n) asm volatile("s_waitcnt vmcnt(" #n ")" ::: "memory")
; #define PG8_WAIT_L(n) asm volatile("s_waitcnt lgkmcnt(" #n ")" ::: "memory")
; #define PG8_BAR __builtin_amdgcn_s_barrier()
; #define PG8_SCHED __builtin_amdgcn_sched_barrier(0)
;     __device__ __forceinline__ void publish(int pm) const { (void)__hip_atomic_fetch_add(zpc + pm, 1u, __ATOMIC_RELAXED, __HIP_MEMORY_SCOPE_AGENT); }
;     __device__ __forceinline__ void publish(int mt) const { (void)__hip_atomic_fetch_add(upc + mt, 1u, __ATOMIC_RELAXED, __HIP_MEMORY_SCOPE_AGENT); }
; template <int K, bool PERM, bool GATHER, int MODE  , class Sched, class Epi>
; __device__ __forceinline__ void gemm_phase(LAS unsigned char* lds, const Sched& S, const Epi& E, const LAS int* gtab, int wv) {
;     ...
;             PG8_LDB(B0, 1, 0); PG8_LDB(B1, 1, 1); PG8_SCHED; PG8_LDA(At, 1, 0); PG8_STAGE_A(PG8_SA(0, 1), a2 + hstep, 1);
;             PG8_WAIT_V(8); PG8_WAIT_L(0); PG8_BAR; PG8_MMA(0, 0, At, B0); PG8_MMA(0, 1, At, B1); PG8_BAR; PG8_SCHED;
;             if constexpr (Epi::PUBLISH) {
;                 if (t == 0 && pmt >= 0) { int tp = tid; asm volatile("" : "+v"(tp)); if (tp == 0) E.publish(pmt); } }
.Lc2_mid:
	v_add_u32_e32 v0, v169, v165
	ds_read_b128 v[12:15], v169
	ds_read_b64 v[16:17], v0 offset:1024
	ds_read_b128 v[18:21], v169 offset:2048
	ds_read_b64 v[22:23], v0 offset:3072
	ds_read_b128 v[0:3], v170
	v_add_u32_e32 v10, v170, v165
	ds_read_b64 v[4:5], v10 offset:1024
	ds_read_b128 v[6:9], v170 offset:2048
	ds_read_b64 v[10:11], v10 offset:3072
	s_mov_b32 m0, s67
	ds_read_b128 v[192:195], v168 offset:32768
	ds_read_b64 v[196:197], v173 offset:33792
	ds_read_b128 v[198:201], v168 offset:34816
	ds_read_b64 v[202:203], v173 offset:35840
	ds_read_b128 v[204:207], v168 offset:36864
	ds_read_b64 v[208:209], v173 offset:37888
	ds_read_b128 v[210:213], v168 offset:38912
	ds_read_b64 v[214:215], v173 offset:39936
	s_nop 0
	global_load_lds_dwordx4 v162, s[24:25]
	s_mov_b32 m0, s73
	s_nop 0
	global_load_lds_dwordx4 v164, s[24:25]
	s_waitcnt vmcnt(8)
	s_waitcnt lgkmcnt(0)
	s_barrier
	s_setprio 1
	s_waitcnt lgkmcnt(0)
	v_mfma_f32_16x16x128_f8f6f4 v[148:151], v[12:17], v[192:197], v[148:151] cbsz:2 blgp:2
	v_mfma_f32_16x16x128_f8f6f4 v[144:147], v[18:23], v[192:197], v[144:147] cbsz:2 blgp:2
	v_mfma_f32_16x16x128_f8f6f4 v[140:143], v[12:17], v[198:203], v[140:143] cbsz:2 blgp:2
	v_mfma_f32_16x16x128_f8f6f4 v[136:139], v[18:23], v[198:203], v[136:139] cbsz:2 blgp:2
	v_mfma_f32_16x16x128_f8f6f4 v[132:135], v[12:17], v[204:209], v[132:135] cbsz:2 blgp:2
	v_mfma_f32_16x16x128_f8f6f4 v[128:131], v[18:23], v[204:209], v[128:131] cbsz:2 blgp:2
	v_mfma_f32_16x16x128_f8f6f4 v[124:127], v[12:17], v[210:215], v[124:127] cbsz:2 blgp:2
	v_mfma_f32_16x16x128_f8f6f4 v[120:123], v[18:23], v[210:215], v[120:123] cbsz:2 blgp:2
	s_setprio 0
	s_setprio 1
	v_mfma_f32_16x16x128_f8f6f4 v[116:119], v[0:5], v[192:197], v[116:119] cbsz:2 blgp:2
	v_mfma_f32_16x16x128_f8f6f4 v[112:115], v[6:11], v[192:197], v[112:115] cbsz:2 blgp:2
	v_mfma_f32_16x16x128_f8f6f4 v[108:111], v[0:5], v[198:203], v[108:111] cbsz:2 blgp:2
	v_mfma_f32_16x16x128_f8f6f4 v[104:107], v[6:11], v[198:203], v[104:107] cbsz:2 blgp:2
	v_mfma_f32_16x16x128_f8f6f4 v[100:103], v[0:5], v[204:209], v[100:103] cbsz:2 blgp:2
	v_mfma_f32_16x16x128_f8f6f4 v[96:99], v[6:11], v[204:209], v[96:99] cbsz:2 blgp:2
	v_mfma_f32_16x16x128_f8f6f4 v[92:95], v[0:5], v[210:215], v[92:95] cbsz:2 blgp:2
	v_mfma_f32_16x16x128_f8f6f4 v[88:91], v[6:11], v[210:215], v[88:91] cbsz:2 blgp:2
	s_setprio 0
	s_barrier
	s_cmp_eq_u32 s20, 0
	s_cselect_b64 s[30:31], -1, 0
	s_and_b64 s[30:31], s[30:31], s[18:19]
	s_andn2_b64 vcc, exec, s[30:31]
	s_cbranch_vccnz .LBB0_746
	v_mov_b32_e32 v152, v154
	s_nop 0
	v_cmp_eq_u32_e32 vcc, 0, v152
	s_and_saveexec_b64 s[30:31], vcc
	s_cbranch_execz .LBB0_745
	s_mov_b64 s[40:41], exec
	v_mbcnt_lo_u32_b32 v152, s40, 0
	v_mbcnt_hi_u32_b32 v152, s41, v152
	v_cmp_eq_u32_e32 vcc, 0, v152
	s_and_b64 s[92:93], exec, vcc
	s_mov_b64 exec, s[92:93]
	s_cbranch_execz .LBB0_745
	s_bcnt1_i32_b64 s40, s[40:41]
	v_mov_b32_e32 v152, s40
	global_atomic_add v153, v152, s[22:23]
	s_branch .LBB0_745

; #define PG8_STAGE_B(bufoff, gbase) do { _Pragma("unroll") for (int _i = 0; _i < 2; ++_i) { unsigned _o = voffB[_i]; asm volatile("" : "+v"(_o)); \
;         __builtin_amdgcn_global_load_lds((const unsigned*)((const char*)(gbase) + _o), (LAS unsigned*)(lds + (bufoff) + ldsw + _i * 8192), 16, 0, 0); } } while (0)
; #define PG8_STAGE_A(bufoff, gbase, h) do { _Pragma("unroll") for (int _i = 0; _i < 2; ++_i) { unsigned _o = (GATHER ? aoffs[h][_i] : voffA[_i]); asm volatile("" : "+v"(_o)); \
;         __builtin_amdgcn_global_load_lds((const unsigned*)((const char*)(gbase) + _o), (LAS unsigned*)(lds + (bufoff) + ldsw + _i * 8192), 16, 0, 0); } } while (0)
; #define PG8_GOFFS(u) do { if constexpr (GATHER) { _Pragma("unroll") for (int _i = 0; _i < 2; ++_i) { int _R, _C; stage_rc(tid * 16 + _i * 8192, _R, _C); \
;         aoffs[0][_i] = (unsigned)gtab[(u) * 256 + _R] * (unsigned)(K * ES) + (unsigned)(_C * 2); aoffs[1][_i] = (unsigned)gtab[(u) * 256 + 128 + _R] * (unsigned)(K * ES) + (unsigned)(_C * 2); } } } while (0)
; #define PG8_WAIT_V(n) asm volatile("s_waitcnt vmcnt(" #n ")" ::: "memory")
; #define PG8_WAIT_L(n) asm volatile("s_waitcnt lgkmcnt(" #n ")" ::: "memory")
; #define PG8_BAR __builtin_amdgcn_s_barrier()
; #define PG8_SCHED __builtin_amdgcn_sched_barrier(0)
; template <int K, bool PERM, bool GATHER, int MODE  , class Sched, class Epi>
; __device__ __forceinline__ void gemm_phase(LAS unsigned char* lds, const Sched& S, const Epi& E, const LAS int* gtab, int wv) {
;     ...
;             PG8_LDB(B0, 0, 0); PG8_LDB(B1, 0, 1); PG8_SCHED; PG8_LDA(At, 0, 0); PG8_STAGE_A(PG8_SA(1, 1), a1 + hstep, 1);
;             PG8_WAIT_V(8); PG8_WAIT_L(0); PG8_BAR; PG8_MMA(0, 0, At, B0); PG8_MMA(0, 1, At, B1); PG8_BAR; PG8_SCHED;
;             if (last && has_next) PG8_GOFFS(ui + 1);
;             PG8_LDA(At, 0, 1); PG8_STAGE_B(PG8_SB(0, 0), b2); PG8_STAGE_B(PG8_SB(0, 1), b2 + BH); PG8_STAGE_A(PG8_SA(0, 0), a2, 0);
;             PG8_WAIT_V(8); PG8_WAIT_L(0); PG8_BAR; PG8_MMA(1, 0, At, B0); PG8_MMA(1, 1, At, B1); PG8_BAR; PG8_SCHED;
;     ...
; #pragma unroll
;         for (int a = 0; a < 2; ++a)
; #pragma unroll
;             for (int b = 0; b < 2; ++b)
; #pragma unroll
;                 for (int m = 0; m < 4; ++m)
; #pragma unroll
;                     for (int n = 0; n < 2; ++n) acc[a][b][m][n] = (f32x4){0.f, 0.f, 0.f, 0.f};
;         pmt = cur.r0 >> 8; cur = nxt; cA = nA; cB = nB; ++ui;
.LBB0_868:
	s_and_b64 s[20:21], s[12:13], exec
	s_cselect_b32 s65, s7, s17
	s_cselect_b32 s66, s6, s16
	s_cselect_b32 s67, s11, s19
	s_cselect_b32 s68, s10, s18
	s_add_u32 s16, s16, 0x20080
	s_addc_u32 s17, s17, 0
	s_add_u32 s69, s18, 0x100
	v_mov_b32_e32 v0, 0
	s_addc_u32 s72, s19, 0
	s_mov_b32 s73, -2
	v_mov_b32_e32 v1, 0
	v_mov_b64_e32 v[2:3], 0
	v_mov_b64_e32 v[4:5], 0
	v_mov_b64_e32 v[6:7], 0
	v_mov_b64_e32 v[8:9], 0
	v_mov_b64_e32 v[10:11], 0
	v_mov_b64_e32 v[12:13], 0
	v_mov_b64_e32 v[14:15], 0
	v_mov_b64_e32 v[16:17], 0
	v_mov_b64_e32 v[18:19], 0
	v_mov_b64_e32 v[20:21], 0
	v_mov_b64_e32 v[22:23], 0
	v_mov_b64_e32 v[24:25], 0
	v_mov_b64_e32 v[26:27], 0
	v_mov_b64_e32 v[28:29], 0
	v_mov_b64_e32 v[30:31], 0
	v_mov_b64_e32 v[64:65], 0
	v_mov_b64_e32 v[66:67], 0
	v_mov_b64_e32 v[68:69], 0
	v_mov_b64_e32 v[70:71], 0
	v_mov_b64_e32 v[72:73], 0
	v_mov_b64_e32 v[74:75], 0
	v_mov_b64_e32 v[76:77], 0
	v_mov_b64_e32 v[78:79], 0
	v_mov_b64_e32 v[80:81], 0
	v_mov_b64_e32 v[82:83], 0
	v_mov_b64_e32 v[84:85], 0
	v_mov_b64_e32 v[86:87], 0
	v_mov_b64_e32 v[88:89], 0
	v_mov_b64_e32 v[90:91], 0
	v_mov_b64_e32 v[92:93], 0
	v_mov_b64_e32 v[94:95], 0
	v_mov_b64_e32 v[32:33], 0
	v_mov_b64_e32 v[34:35], 0
	v_mov_b64_e32 v[36:37], 0
	v_mov_b64_e32 v[38:39], 0
	v_mov_b64_e32 v[40:41], 0
	v_mov_b64_e32 v[42:43], 0
	v_mov_b64_e32 v[44:45], 0
	v_mov_b64_e32 v[46:47], 0
	v_mov_b64_e32 v[48:49], 0
	v_mov_b64_e32 v[50:51], 0
	v_mov_b64_e32 v[52:53], 0
	v_mov_b64_e32 v[54:55], 0
	v_mov_b64_e32 v[56:57], 0
	v_mov_b64_e32 v[58:59], 0
	v_mov_b64_e32 v[60:61], 0
	v_mov_b64_e32 v[62:63], 0
	v_mov_b64_e32 v[96:97], 0
	v_mov_b64_e32 v[98:99], 0
	v_mov_b64_e32 v[100:101], 0
	v_mov_b64_e32 v[102:103], 0
	v_mov_b64_e32 v[104:105], 0
	v_mov_b64_e32 v[106:107], 0
	v_mov_b64_e32 v[108:109], 0
	v_mov_b64_e32 v[110:111], 0
	v_mov_b64_e32 v[112:113], 0
	v_mov_b64_e32 v[114:115], 0
	v_mov_b64_e32 v[116:117], 0
	v_mov_b64_e32 v[118:119], 0
	v_mov_b64_e32 v[120:121], 0
	v_mov_b64_e32 v[122:123], 0
	v_mov_b64_e32 v[124:125], 0
	v_mov_b64_e32 v[126:127], 0
	s_cmp_eq_u32 s57, 1
	s_cbranch_scc1 .LBB0_869
	s_add_u32 s18, s16, 0xfffe0080
	s_addc_u32 s19, s17, -1
	s_add_i32 s74, 0, 0x10000
	s_cmp_eq_u32 s73, 4
	s_cselect_b32 s19, s65, s19
	s_cselect_b32 s18, s66, s18
	v_add_u32_e32 v143, s74, v141
	s_cselect_b32 s21, s67, s72
	s_cselect_b32 s20, s68, s69
	s_add_i32 s76, 0, 0x14000
	ds_read_b128 v[128:131], v143
	ds_read_b128 v[132:135], v143 offset:1024
	ds_read_b128 v[144:147], v143 offset:2048
	ds_read_b128 v[148:151], v143 offset:3072
	v_add_u32_e32 v143, s76, v141
	ds_read_b128 v[154:157], v143
	ds_read_b128 v[158:161], v143 offset:1024
	ds_read_b128 v[162:165], v143 offset:2048
	ds_read_b128 v[166:169], v143 offset:3072
	v_mov_b32_e32 v143, v137
	ds_read_b128 v[170:173], v142
	ds_read_b128 v[174:177], v142 offset:1024
	ds_read_b128 v[192:195], v142 offset:2048
	ds_read_b128 v[196:199], v142 offset:3072
	ds_read_b128 v[200:203], v142 offset:4096
	ds_read_b128 v[204:207], v142 offset:5120
	ds_read_b128 v[208:211], v142 offset:6144
	ds_read_b128 v[212:215], v142 offset:7168
	s_add_i32 m0, s15, 0xc000
	s_nop 0
	global_load_lds_dwordx4 v143, s[16:17]
	v_mov_b32_e32 v143, v139
	s_add_i32 m0, s15, 0xe000
	s_nop 0
	global_load_lds_dwordx4 v143, s[16:17]
	s_waitcnt vmcnt(16)
	s_waitcnt lgkmcnt(0)
	s_barrier
	s_setprio 1
	s_waitcnt lgkmcnt(0)
	v_mfma_f32_16x16x128_f8f6f4 v[124:127], v[128:135], v[170:177], v[124:127]
	v_mfma_f32_16x16x128_f8f6f4 v[120:123], v[144:151], v[170:177], v[120:123]
	v_mfma_f32_16x16x128_f8f6f4 v[116:119], v[128:135], v[192:199], v[116:119]
	v_mfma_f32_16x16x128_f8f6f4 v[112:115], v[144:151], v[192:199], v[112:115]
	v_mfma_f32_16x16x128_f8f6f4 v[108:111], v[128:135], v[200:207], v[108:111]
	v_mfma_f32_16x16x128_f8f6f4 v[104:107], v[144:151], v[200:207], v[104:107]
	v_mfma_f32_16x16x128_f8f6f4 v[100:103], v[128:135], v[208:215], v[100:103]
	v_mfma_f32_16x16x128_f8f6f4 v[96:99], v[144:151], v[208:215], v[96:99]
	s_setprio 0
	s_setprio 1
	v_mfma_f32_16x16x128_f8f6f4 v[178:181], v[154:161], v[170:177], v[60:63]
	v_mfma_f32_16x16x128_f8f6f4 v[170:173], v[162:169], v[170:177], v[56:59]
	v_mfma_f32_16x16x128_f8f6f4 v[174:177], v[154:161], v[192:199], v[52:55]
	v_mfma_f32_16x16x128_f8f6f4 v[192:195], v[162:169], v[192:199], v[48:51]
	v_mfma_f32_16x16x128_f8f6f4 v[196:199], v[154:161], v[200:207], v[44:47]
	v_mfma_f32_16x16x128_f8f6f4 v[200:203], v[162:169], v[200:207], v[40:43]
	v_mfma_f32_16x16x128_f8f6f4 v[204:207], v[154:161], v[208:215], v[36:39]
	v_mfma_f32_16x16x128_f8f6f4 v[208:211], v[162:169], v[208:215], v[32:35]
	s_setprio 0
	s_barrier
	v_mov_b32_e32 v143, v138
	s_add_i32 s74, s74, s28
	s_nop 2
	ds_read_b128 v[32:35], v142 offset:16384
	ds_read_b128 v[36:39], v142 offset:17408
	ds_read_b128 v[40:43], v142 offset:18432
	ds_read_b128 v[44:47], v142 offset:19456
	ds_read_b128 v[48:51], v142 offset:20480
	ds_read_b128 v[52:55], v142 offset:21504
	ds_read_b128 v[56:59], v142 offset:22528
	ds_read_b128 v[60:63], v142 offset:23552
	s_mov_b32 m0, s74
	s_nop 0
	global_load_lds_dwordx4 v143, s[20:21]
	v_mov_b32_e32 v143, v140
	s_add_i32 m0, s74, 0x2000
	s_add_u32 s74, s20, 0x20000
	global_load_lds_dwordx4 v143, s[20:21]
	s_addc_u32 s75, s21, 0
	v_mov_b32_e32 v143, v138
	s_add_i32 s76, s76, s28
	s_mov_b32 m0, s76
	s_nop 0
	global_load_lds_dwordx4 v143, s[74:75]
	v_mov_b32_e32 v143, v140
	s_add_i32 m0, s76, 0x2000
	s_nop 0
	global_load_lds_dwordx4 v143, s[74:75]
	v_mov_b32_e32 v143, v137
	s_mov_b32 m0, s15
	s_nop 0
	global_load_lds_dwordx4 v143, s[18:19]
	v_mov_b32_e32 v143, v139
	s_mov_b32 m0, s30
	s_nop 0
	global_load_lds_dwordx4 v143, s[18:19]
	s_waitcnt vmcnt(16)
	s_waitcnt lgkmcnt(0)
	s_barrier
	s_setprio 1
	s_waitcnt lgkmcnt(0)
	v_mfma_f32_16x16x128_f8f6f4 v[92:95], v[128:135], v[32:39], v[92:95]
	v_mfma_f32_16x16x128_f8f6f4 v[88:91], v[144:151], v[32:39], v[88:91]
	v_mfma_f32_16x16x128_f8f6f4 v[84:87], v[128:135], v[40:47], v[84:87]
	v_mfma_f32_16x16x128_f8f6f4 v[80:83], v[144:151], v[40:47], v[80:83]
	v_mfma_f32_16x16x128_f8f6f4 v[76:79], v[128:135], v[48:55], v[76:79]
	v_mfma_f32_16x16x128_f8f6f4 v[72:75], v[144:151], v[48:55], v[72:75]
	v_mfma_f32_16x16x128_f8f6f4 v[212:215], v[128:135], v[56:63], v[68:71]
	v_mfma_f32_16x16x128_f8f6f4 v[216:219], v[144:151], v[56:63], v[64:67]
	s_setprio 0
	s_setprio 1
	v_mfma_f32_16x16x128_f8f6f4 v[220:223], v[154:161], v[32:39], v[28:31]
	v_mfma_f32_16x16x128_f8f6f4 v[224:227], v[162:169], v[32:39], v[24:27]
	v_mfma_f32_16x16x128_f8f6f4 v[228:231], v[154:161], v[40:47], v[20:23]
	v_mfma_f32_16x16x128_f8f6f4 v[232:235], v[162:169], v[40:47], v[16:19]
	v_mfma_f32_16x16x128_f8f6f4 v[236:239], v[154:161], v[48:55], v[12:15]
	v_mfma_f32_16x16x128_f8f6f4 v[240:243], v[162:169], v[48:55], v[8:11]
	v_mfma_f32_16x16x128_f8f6f4 v[244:247], v[154:161], v[56:63], v[4:7]
	v_mfma_f32_16x16x128_f8f6f4 v[248:251], v[162:169], v[56:63], v[0:3]
	s_setprio 0
	s_barrier
	s_branch .Lc3_mid

; #define PG8_STAGE_B(bufoff, gbase) do { _Pragma("unroll") for (int _i = 0; _i < 2; ++_i) { unsigned _o = voffB[_i]; asm volatile("" : "+v"(_o)); \
;         __builtin_amdgcn_global_load_lds((const unsigned*)((const char*)(gbase) + _o), (LAS unsigned*)(lds + (bufoff) + ldsw + _i * 8192), 16, 0, 0); } } while (0)
; #define PG8_STAGE_A(bufoff, gbase, h) do { _Pragma("unroll") for (int _i = 0; _i < 2; ++_i) { unsigned _o = (GATHER ? aoffs[h][_i] : voffA[_i]); asm volatile("" : "+v"(_o)); \
;         __builtin_amdgcn_global_load_lds((const unsigned*)((const char*)(gbase) + _o), (LAS unsigned*)(lds + (bufoff) + ldsw + _i * 8192), 16, 0, 0); } } while (0)
; #define PG8_WAIT_V(n) asm volatile("s_waitcnt vmcnt(" #n ")" ::: "memory")
; #define PG8_WAIT_L(n) asm volatile("s_waitcnt lgkmcnt(" #n ")" ::: "memory")
; #define PG8_BAR __builtin_amdgcn_s_barrier()
; #define PG8_SCHED __builtin_amdgcn_sched_barrier(0)
;     __device__ __forceinline__ void publish(int pm) const { (void)__hip_atomic_fetch_add(zpc + pm, 1u, __ATOMIC_RELAXED, __HIP_MEMORY_SCOPE_AGENT); }
;     __device__ __forceinline__ void publish(int mt) const { (void)__hip_atomic_fetch_add(upc + mt, 1u, __ATOMIC_RELAXED, __HIP_MEMORY_SCOPE_AGENT); }
; template <int K, bool PERM, bool GATHER, int MODE  , class Sched, class Epi>
; __device__ __forceinline__ void gemm_phase(LAS unsigned char* lds, const Sched& S, const Epi& E, const LAS int* gtab, int wv) {
;     ...
;             PG8_LDB(B0, 1, 0); PG8_LDB(B1, 1, 1); PG8_SCHED; PG8_LDA(At, 1, 0); PG8_STAGE_A(PG8_SA(0, 1), a2 + hstep, 1);
;             PG8_WAIT_V(8); PG8_WAIT_L(0); PG8_BAR; PG8_MMA(0, 0, At, B0); PG8_MMA(0, 1, At, B1); PG8_BAR; PG8_SCHED;
;             if constexpr (Epi::PUBLISH) {
;                 if (t == 0 && pmt >= 0) { int tp = tid; asm volatile("" : "+v"(tp)); if (tp == 0) E.publish(pmt); } }
;             PG8_LDA(At, 1, 1); PG8_STAGE_B(PG8_SB(1, 0), b3); PG8_STAGE_B(PG8_SB(1, 1), b3 + BH); PG8_STAGE_A(PG8_SA(1, 0), a3, 0);
;             PG8_WAIT_V(8); PG8_WAIT_L(0); PG8_BAR; PG8_MMA(1, 0, At, B0); PG8_MMA(1, 1, At, B1); PG8_BAR; PG8_SCHED;
;         }
.Lc3_mid:
	s_nop 1
	v_add_u32_e32 v12, s81, v141
	v_add_u32_e32 v16, s45, v141
	s_nop 0
	ds_read_b128 v[0:3], v12
	ds_read_b128 v[4:7], v12 offset:1024
	ds_read_b128 v[8:11], v12 offset:2048
	ds_read_b128 v[12:15], v12 offset:3072
	ds_read_b128 v[128:131], v16
	ds_read_b128 v[132:135], v16 offset:1024
	ds_read_b128 v[144:147], v16 offset:2048
	ds_read_b128 v[148:151], v16 offset:3072
	s_add_u32 s74, s18, 0x20000
	v_mov_b32_e32 v40, v137
	s_mov_b32 m0, s31
	ds_read_b128 v[16:19], v142 offset:32768
	ds_read_b128 v[20:23], v142 offset:33792
	ds_read_b128 v[24:27], v142 offset:34816
	ds_read_b128 v[28:31], v142 offset:35840
	ds_read_b128 v[32:35], v142 offset:36864
	ds_read_b128 v[36:39], v142 offset:37888
	ds_read_b128 v[64:67], v142 offset:38912
	ds_read_b128 v[68:71], v142 offset:39936
	s_addc_u32 s75, s19, 0
	s_nop 0
	global_load_lds_dwordx4 v40, s[74:75]
	v_mov_b32_e32 v40, v139
	s_mov_b32 m0, s33
	s_nop 0
	global_load_lds_dwordx4 v40, s[74:75]
	s_waitcnt vmcnt(8)
	s_waitcnt lgkmcnt(0)
	s_barrier
	s_setprio 1
	s_waitcnt lgkmcnt(0)
	v_mfma_f32_16x16x128_f8f6f4 v[124:127], v[0:7], v[16:23], v[124:127]
	v_mfma_f32_16x16x128_f8f6f4 v[120:123], v[8:15], v[16:23], v[120:123]
	v_mfma_f32_16x16x128_f8f6f4 v[116:119], v[0:7], v[24:31], v[116:119]
	v_mfma_f32_16x16x128_f8f6f4 v[112:115], v[8:15], v[24:31], v[112:115]
	v_mfma_f32_16x16x128_f8f6f4 v[108:111], v[0:7], v[32:39], v[108:111]
	v_mfma_f32_16x16x128_f8f6f4 v[104:107], v[8:15], v[32:39], v[104:107]
	v_mfma_f32_16x16x128_f8f6f4 v[100:103], v[0:7], v[64:71], v[100:103]
	v_mfma_f32_16x16x128_f8f6f4 v[96:99], v[8:15], v[64:71], v[96:99]
	s_setprio 0
	s_setprio 1
	v_mfma_f32_16x16x128_f8f6f4 v[60:63], v[128:135], v[16:23], v[178:181]
	v_mfma_f32_16x16x128_f8f6f4 v[56:59], v[144:151], v[16:23], v[170:173]
	v_mfma_f32_16x16x128_f8f6f4 v[52:55], v[128:135], v[24:31], v[174:177]
	v_mfma_f32_16x16x128_f8f6f4 v[48:51], v[144:151], v[24:31], v[192:195]
	v_mfma_f32_16x16x128_f8f6f4 v[44:47], v[128:135], v[32:39], v[196:199]
	v_mfma_f32_16x16x128_f8f6f4 v[40:43], v[144:151], v[32:39], v[200:203]
	v_mfma_f32_16x16x128_f8f6f4 v[36:39], v[128:135], v[64:71], v[204:207]
	v_mfma_f32_16x16x128_f8f6f4 v[32:35], v[144:151], v[64:71], v[208:211]
	s_setprio 0
	s_barrier
	v_mov_b32_e32 v152, v138
	ds_read_b128 v[16:19], v142 offset:49152
	ds_read_b128 v[20:23], v142 offset:50176
	ds_read_b128 v[154:157], v142 offset:51200
	ds_read_b128 v[158:161], v142 offset:52224
	ds_read_b128 v[162:165], v142 offset:53248
	ds_read_b128 v[166:169], v142 offset:54272
	ds_read_b128 v[170:173], v142 offset:55296
	ds_read_b128 v[174:177], v142 offset:56320
	s_add_i32 s74, s81, s28
	v_lshl_add_u64 v[24:25], s[20:21], 0, v[152:153]
	v_lshl_add_u64 v[24:25], v[24:25], 0, s[34:35]
	s_mov_b32 m0, s74
	v_mov_b32_e32 v152, v140
	global_load_lds_dwordx4 v[24:25], off
	s_add_i32 m0, s74, 0x2000
	v_lshl_add_u64 v[24:25], s[20:21], 0, v[152:153]
	v_lshl_add_u64 v[24:25], v[24:25], 0, s[34:35]
	s_add_u32 s20, s20, 0x20080
	global_load_lds_dwordx4 v[24:25], off
	s_addc_u32 s21, s21, 0
	v_mov_b32_e32 v24, v138
	s_add_i32 s74, s45, s28
	s_mov_b32 m0, s74
	v_mov_b32_e32 v152, v137
	global_load_lds_dwordx4 v24, s[20:21]
	v_mov_b32_e32 v24, v140
	s_add_i32 m0, s74, 0x2000
	s_nop 0
	global_load_lds_dwordx4 v24, s[20:21]
	s_mov_b32 m0, s40
	v_lshl_add_u64 v[24:25], s[18:19], 0, v[152:153]
	v_lshl_add_u64 v[24:25], v[24:25], 0, s[34:35]
	v_mov_b32_e32 v152, v139
	global_load_lds_dwordx4 v[24:25], off
	s_mov_b32 m0, s41
	v_lshl_add_u64 v[24:25], s[18:19], 0, v[152:153]
	v_lshl_add_u64 v[24:25], v[24:25], 0, s[34:35]
	global_load_lds_dwordx4 v[24:25], off
	s_waitcnt vmcnt(8)
	s_waitcnt lgkmcnt(0)
	s_barrier
	s_setprio 1
	s_waitcnt lgkmcnt(0)
	v_mfma_f32_16x16x128_f8f6f4 v[92:95], v[0:7], v[16:23], v[92:95]
	v_mfma_f32_16x16x128_f8f6f4 v[88:91], v[8:15], v[16:23], v[88:91]
	v_mfma_f32_16x16x128_f8f6f4 v[84:87], v[0:7], v[154:161], v[84:87]
	v_mfma_f32_16x16x128_f8f6f4 v[80:83], v[8:15], v[154:161], v[80:83]
	v_mfma_f32_16x16x128_f8f6f4 v[76:79], v[0:7], v[162:169], v[76:79]
	v_mfma_f32_16x16x128_f8f6f4 v[72:75], v[8:15], v[162:169], v[72:75]
	v_mfma_f32_16x16x128_f8f6f4 v[68:71], v[0:7], v[170:177], v[212:215]
	v_mfma_f32_16x16x128_f8f6f4 v[64:67], v[8:15], v[170:177], v[216:219]
	s_setprio 0
	s_setprio 1
	v_mfma_f32_16x16x128_f8f6f4 v[28:31], v[128:135], v[16:23], v[220:223]
	v_mfma_f32_16x16x128_f8f6f4 v[24:27], v[144:151], v[16:23], v[224:227]
	v_mfma_f32_16x16x128_f8f6f4 v[20:23], v[128:135], v[154:161], v[228:231]
	v_mfma_f32_16x16x128_f8f6f4 v[16:19], v[144:151], v[154:161], v[232:235]
	v_mfma_f32_16x16x128_f8f6f4 v[12:15], v[128:135], v[162:169], v[236:239]
	v_mfma_f32_16x16x128_f8f6f4 v[8:11], v[144:151], v[162:169], v[240:243]
	v_mfma_f32_16x16x128_f8f6f4 v[4:7], v[128:135], v[170:177], v[244:247]
	v_mfma_f32_16x16x128_f8f6f4 v[0:3], v[144:151], v[170:177], v[248:251]
	s_setprio 0
	s_barrier
	s_add_i32 s73, s73, 2
	s_add_u32 s16, s16, 0x100
	s_addc_u32 s17, s17, 0
	s_add_u32 s69, s69, 0x100
	s_addc_u32 s72, s72, 0
	s_cmp_gt_u32 s73, 5
	s_cbranch_scc0 .LBB0_869
	s_and_b64 vcc, exec, s[4:5]
	s_cbranch_vccz .LBB0_872
	s_barrier
